# stack12 + PRO position-term loop software-pipelined (next trip's 20 loads issued before the current trip's fmacs, two register sets), same accumulation order
# speedup vs baseline: 1.0002x; 1.0002x over previous
.LBB0_89:
	s_add_u32 s16, s2, s6
	s_addc_u32 s17, s15, s7
	global_load_dwordx4 v[8:11], v3, s[16:17] offset:48
	global_load_dwordx4 v[12:15], v3, s[16:17] offset:32
	global_load_dwordx4 v[16:19], v3, s[16:17] offset:16
	global_load_dwordx4 v[20:23], v3, s[16:17]
	v_add_co_u32_e32 v228, vcc, s10, v4
	s_nop 1
	v_addc_co_u32_e32 v229, vcc, -1, v5, vcc
	global_load_dword v7, v[228:229], off offset:-3072
	global_load_dword v28, v[228:229], off offset:-2048
	global_load_dword v29, v[228:229], off offset:-1024
	v_add_co_u32_e32 v230, vcc, s11, v4
	s_nop 1
	v_addc_co_u32_e32 v231, vcc, -1, v5, vcc
	global_load_dword v30, v[230:231], off offset:-4096
	global_load_dword v31, v[230:231], off offset:-3072
	global_load_dword v32, v[230:231], off offset:-2048
	global_load_dword v33, v[230:231], off offset:-1024
	global_load_dword v34, v[230:231], off
	v_add_co_u32_e32 v232, vcc, s12, v4
	s_nop 1
	v_addc_co_u32_e32 v233, vcc, -1, v5, vcc
	global_load_dword v26, v[232:233], off offset:-3072
	global_load_dword v27, v[232:233], off offset:-2048
	global_load_dword v35, v[232:233], off offset:-1024
	global_load_dword v36, v[4:5], off offset:-4096
	global_load_dword v37, v[4:5], off offset:-3072
	global_load_dword v38, v[4:5], off offset:-2048
	global_load_dword v39, v[4:5], off offset:-1024
	global_load_dword v40, v[4:5], off
	s_add_u32 s6, s6, 64
	s_addc_u32 s7, s7, 0
	v_lshl_add_u64 v[4:5], v[4:5], 0, s[4:5]
	s_mov_b32 s100, 15
.Lpt_loop:
	s_add_u32 s16, s2, s6
	s_addc_u32 s17, s15, s7
	global_load_dwordx4 v[208:211], v3, s[16:17] offset:48
	global_load_dwordx4 v[204:207], v3, s[16:17] offset:32
	global_load_dwordx4 v[200:203], v3, s[16:17] offset:16
	global_load_dwordx4 v[196:199], v3, s[16:17]
	v_add_co_u32_e32 v228, vcc, s10, v4
	s_nop 1
	v_addc_co_u32_e32 v229, vcc, -1, v5, vcc
	global_load_dword v212, v[228:229], off offset:-3072
	global_load_dword v213, v[228:229], off offset:-2048
	global_load_dword v214, v[228:229], off offset:-1024
	v_add_co_u32_e32 v230, vcc, s11, v4
	s_nop 1
	v_addc_co_u32_e32 v231, vcc, -1, v5, vcc
	global_load_dword v215, v[230:231], off offset:-4096
	global_load_dword v216, v[230:231], off offset:-3072
	global_load_dword v217, v[230:231], off offset:-2048
	global_load_dword v218, v[230:231], off offset:-1024
	global_load_dword v219, v[230:231], off
	v_add_co_u32_e32 v232, vcc, s12, v4
	s_nop 1
	v_addc_co_u32_e32 v233, vcc, -1, v5, vcc
	global_load_dword v220, v[232:233], off offset:-3072
	global_load_dword v221, v[232:233], off offset:-2048
	global_load_dword v222, v[232:233], off offset:-1024
	global_load_dword v223, v[4:5], off offset:-4096
	global_load_dword v224, v[4:5], off offset:-3072
	global_load_dword v225, v[4:5], off offset:-2048
	global_load_dword v226, v[4:5], off offset:-1024
	global_load_dword v227, v[4:5], off
	s_add_u32 s6, s6, 64
	s_addc_u32 s7, s7, 0
	v_lshl_add_u64 v[4:5], v[4:5], 0, s[4:5]
	s_waitcnt vmcnt(20)
	v_fmac_f32_e32 v6, v20, v7
	v_fmac_f32_e32 v6, v21, v28
	v_fmac_f32_e32 v6, v22, v29
	v_fmac_f32_e32 v6, v23, v30
	v_fmac_f32_e32 v6, v16, v31
	v_fmac_f32_e32 v6, v17, v32
	v_fmac_f32_e32 v6, v18, v33
	v_fmac_f32_e32 v6, v19, v34
	v_fmac_f32_e32 v6, v12, v26
	v_fmac_f32_e32 v6, v13, v27
	v_fmac_f32_e32 v6, v14, v35
	v_fmac_f32_e32 v6, v15, v36
	v_fmac_f32_e32 v6, v8, v37
	v_fmac_f32_e32 v6, v9, v38
	v_fmac_f32_e32 v6, v10, v39
	v_fmac_f32_e32 v6, v11, v40
	s_add_u32 s16, s2, s6
	s_addc_u32 s17, s15, s7
	global_load_dwordx4 v[8:11], v3, s[16:17] offset:48
	global_load_dwordx4 v[12:15], v3, s[16:17] offset:32
	global_load_dwordx4 v[16:19], v3, s[16:17] offset:16
	global_load_dwordx4 v[20:23], v3, s[16:17]
	v_add_co_u32_e32 v228, vcc, s10, v4
	s_nop 1
	v_addc_co_u32_e32 v229, vcc, -1, v5, vcc
	global_load_dword v7, v[228:229], off offset:-3072
	global_load_dword v28, v[228:229], off offset:-2048
	global_load_dword v29, v[228:229], off offset:-1024
	v_add_co_u32_e32 v230, vcc, s11, v4
	s_nop 1
	v_addc_co_u32_e32 v231, vcc, -1, v5, vcc
	global_load_dword v30, v[230:231], off offset:-4096
	global_load_dword v31, v[230:231], off offset:-3072
	global_load_dword v32, v[230:231], off offset:-2048
	global_load_dword v33, v[230:231], off offset:-1024
	global_load_dword v34, v[230:231], off
	v_add_co_u32_e32 v232, vcc, s12, v4
	s_nop 1
	v_addc_co_u32_e32 v233, vcc, -1, v5, vcc
	global_load_dword v26, v[232:233], off offset:-3072
	global_load_dword v27, v[232:233], off offset:-2048
	global_load_dword v35, v[232:233], off offset:-1024
	global_load_dword v36, v[4:5], off offset:-4096
	global_load_dword v37, v[4:5], off offset:-3072
	global_load_dword v38, v[4:5], off offset:-2048
	global_load_dword v39, v[4:5], off offset:-1024
	global_load_dword v40, v[4:5], off
	s_add_u32 s6, s6, 64
	s_addc_u32 s7, s7, 0
	v_lshl_add_u64 v[4:5], v[4:5], 0, s[4:5]
	s_waitcnt vmcnt(20)
	v_fmac_f32_e32 v6, v196, v212
	v_fmac_f32_e32 v6, v197, v213
	v_fmac_f32_e32 v6, v198, v214
	v_fmac_f32_e32 v6, v199, v215
	v_fmac_f32_e32 v6, v200, v216
	v_fmac_f32_e32 v6, v201, v217
	v_fmac_f32_e32 v6, v202, v218
	v_fmac_f32_e32 v6, v203, v219
	v_fmac_f32_e32 v6, v204, v220
	v_fmac_f32_e32 v6, v205, v221
	v_fmac_f32_e32 v6, v206, v222
	v_fmac_f32_e32 v6, v207, v223
	v_fmac_f32_e32 v6, v208, v224
	v_fmac_f32_e32 v6, v209, v225
	v_fmac_f32_e32 v6, v210, v226
	v_fmac_f32_e32 v6, v211, v227
	s_sub_u32 s100, s100, 1
	s_cmp_lg_u32 s100, 0
	s_cbranch_scc1 .Lpt_loop
	s_add_u32 s16, s2, s6
	s_addc_u32 s17, s15, s7
	global_load_dwordx4 v[208:211], v3, s[16:17] offset:48
	global_load_dwordx4 v[204:207], v3, s[16:17] offset:32
	global_load_dwordx4 v[200:203], v3, s[16:17] offset:16
	global_load_dwordx4 v[196:199], v3, s[16:17]
	v_add_co_u32_e32 v228, vcc, s10, v4
	s_nop 1
	v_addc_co_u32_e32 v229, vcc, -1, v5, vcc
	global_load_dword v212, v[228:229], off offset:-3072
	global_load_dword v213, v[228:229], off offset:-2048
	global_load_dword v214, v[228:229], off offset:-1024
	v_add_co_u32_e32 v230, vcc, s11, v4
	s_nop 1
	v_addc_co_u32_e32 v231, vcc, -1, v5, vcc
	global_load_dword v215, v[230:231], off offset:-4096
	global_load_dword v216, v[230:231], off offset:-3072
	global_load_dword v217, v[230:231], off offset:-2048
	global_load_dword v218, v[230:231], off offset:-1024
	global_load_dword v219, v[230:231], off
	v_add_co_u32_e32 v232, vcc, s12, v4
	s_nop 1
	v_addc_co_u32_e32 v233, vcc, -1, v5, vcc
	global_load_dword v220, v[232:233], off offset:-3072
	global_load_dword v221, v[232:233], off offset:-2048
	global_load_dword v222, v[232:233], off offset:-1024
	global_load_dword v223, v[4:5], off offset:-4096
	global_load_dword v224, v[4:5], off offset:-3072
	global_load_dword v225, v[4:5], off offset:-2048
	global_load_dword v226, v[4:5], off offset:-1024
	global_load_dword v227, v[4:5], off
	s_add_u32 s6, s6, 64
	s_addc_u32 s7, s7, 0
	v_lshl_add_u64 v[4:5], v[4:5], 0, s[4:5]
	s_waitcnt vmcnt(20)
	v_fmac_f32_e32 v6, v20, v7
	v_fmac_f32_e32 v6, v21, v28
	v_fmac_f32_e32 v6, v22, v29
	v_fmac_f32_e32 v6, v23, v30
	v_fmac_f32_e32 v6, v16, v31
	v_fmac_f32_e32 v6, v17, v32
	v_fmac_f32_e32 v6, v18, v33
	v_fmac_f32_e32 v6, v19, v34
	v_fmac_f32_e32 v6, v12, v26
	v_fmac_f32_e32 v6, v13, v27
	v_fmac_f32_e32 v6, v14, v35
	v_fmac_f32_e32 v6, v15, v36
	v_fmac_f32_e32 v6, v8, v37
	v_fmac_f32_e32 v6, v9, v38
	v_fmac_f32_e32 v6, v10, v39
	v_fmac_f32_e32 v6, v11, v40
	s_waitcnt vmcnt(0)
	v_fmac_f32_e32 v6, v196, v212
	v_fmac_f32_e32 v6, v197, v213
	v_fmac_f32_e32 v6, v198, v214
	v_fmac_f32_e32 v6, v199, v215
	v_fmac_f32_e32 v6, v200, v216
	v_fmac_f32_e32 v6, v201, v217
	v_fmac_f32_e32 v6, v202, v218
	v_fmac_f32_e32 v6, v203, v219
	v_fmac_f32_e32 v6, v204, v220
	v_fmac_f32_e32 v6, v205, v221
	v_fmac_f32_e32 v6, v206, v222
	v_fmac_f32_e32 v6, v207, v223
	v_fmac_f32_e32 v6, v208, v224
	v_fmac_f32_e32 v6, v209, v225
	v_fmac_f32_e32 v6, v210, v226
	v_fmac_f32_e32 v6, v211, v227
	s_and_b32 s2, s14, 7
	s_and_b32 s6, s14, 0xfffff8
	s_or_b32 s2, s6, s2
	v_lshl_or_b32 v4, s2, 8, v1
	v_ashrrev_i32_e32 v5, 31, v4
	s_add_i32 s13, s13, s66
	v_lshl_add_u64 v[4:5], v[4:5], 2, s[0:1]
	s_cmp_gt_i32 s13, 63
	global_store_dword v[4:5], v6, off
	s_cbranch_scc0 .LBB0_88
